# final combine streaming loads/stores marked nt so the early pass does not evict the tail GEMM's weight tiles from L2
# speedup vs baseline: 1.0232x; 1.0151x over previous
; __device__ __forceinline__ float bf_lo(unsigned w) { return __uint_as_float(w << 16); }
; __device__ __forceinline__ float bf_hi(unsigned w) { return __uint_as_float(w & 0xffff0000u); }
; __device__ __forceinline__ f32x4 ld4_bf(const bf16_t* p) { const u32x2 w = *(const u32x2*)p; return (f32x4){bf_lo(w.x), bf_hi(w.x), bf_lo(w.y), bf_hi(w.y)}; }
; __device__ __forceinline__ float sq4(const f32x4 v) { return (v[0] * v[0] + v[1] * v[1]) + (v[2] * v[2] + v[3] * v[3]); }
; __device__ __forceinline__ void phase_final(const Ctx& P, volatile LAS int* tab, int vcu, int G) {
;     ...
;     for (int row = gw; row < ML; row += NGW) {
;         const int e1 = tok[row * 8], pos1 = tok[row * 8 + 1], e2 = tok[row * 8 + 2], pos2 = tok[row * 8 + 3]; const float p1 = ((const float*)tok)[row * 8 + 4], p2 = ((const float*)tok)[row * 8 + 5];
;         const bf16_t* y1 = YB + (size_t)(tab[8 + e1] * 256 + pos1) * DM; const bf16_t* y2 = YB + (size_t)(tab[8 + e2] * 256 + pos2) * DM;
;         const bf16_t* xr = (const bf16_t*)(P.ws + WS_XA) + (size_t)row * DM; const float* g2 = mod + (size_t)(row >> 12) * NMOD + 5 * DM;
;         f32x4 v[8]; float ss = 0.f;
; #pragma unroll
;         for (int j = 0; j < 8; ++j) { const int c = 4 * lane + 256 * j; const f32x4 x4 = ld4_bf(xr + c), g4 = *(const f32x4*)(g2 + c); const u32x2 a = *(const u32x2*)(y1 + c), b = *(const u32x2*)(y2 + c);
;             const f32x4 ya = (f32x4){bf_lo(a.x), bf_hi(a.x), bf_lo(a.y), bf_hi(a.y)}, yb = (f32x4){bf_lo(b.x), bf_hi(b.x), bf_lo(b.y), bf_hi(b.y)};
;             v[j] = x4 + g4 * (ya * p1 + yb * p2); ss += sq4(v[j]); }
.LBB0_2712:
	v_mov_b32_e32 v16, v194
	v_mov_b32_e32 v17, v195
	v_mov_b32_e32 v18, v196
	v_mov_b32_e32 v19, v197
	v_mov_b32_e32 v46, v198
	v_mov_b32_e32 v47, v199
	v_max_i32_e32 v200, v194, v196
	s_ashr_i32 s3, s10, 12
	s_mul_hi_i32 s8, s3, 0xc000
	s_mul_i32 s3, s3, 0xc000
	s_add_u32 s3, s36, s3
	s_addc_u32 s9, s37, s8
	s_add_u32 s8, s3, 0x146000
	s_addc_u32 s9, s9, 0
	s_add_i32 s10, s10, s0
	s_add_i32 s2, s2, s13
	s_ashr_i32 s3, s2, 31
	s_lshl_b64 s[14:15], s[2:3], 2
	s_add_u32 s14, s11, s14
	s_addc_u32 s15, s12, s15
	s_cmpk_lt_i32 s10, 0x4000
	s_cselect_b32 s17, 1, 0
	v_readfirstlane_b32 s16, v200
	s_cmp_lt_i32 s16, s20
	s_cbranch_scc1 .Lp16_skip
	s_cmp_ge_i32 s16, s21
	s_cbranch_scc1 .Lp16_skip
	v_lshlrev_b32_e32 v0, 2, v16
	v_lshlrev_b32_e32 v1, 2, v18
	v_add_u32_e32 v0, s1, v0
	v_add_u32_e32 v1, s1, v1
	ds_read_b32 v16, v0 offset:32
	ds_read_b32 v18, v1 offset:32
	global_load_dwordx2 v[48:49], v[34:35], off offset:-2048 nt
	global_load_dwordx2 v[50:51], v[34:35], off offset:-1536 nt
	global_load_dwordx2 v[52:53], v[34:35], off offset:-1024 nt
	global_load_dwordx4 v[0:3], v28, s[8:9]
	global_load_dwordx2 v[54:55], v[34:35], off offset:-512 nt
	global_load_dwordx4 v[8:11], v64, s[8:9]
	global_load_dwordx4 v[4:7], v65, s[8:9]
	global_load_dwordx4 v[12:15], v66, s[8:9]
	global_load_dwordx2 v[56:57], v[34:35], off nt
	global_load_dwordx4 v[20:23], v36, s[8:9]
	global_load_dwordx4 v[24:27], v38, s[8:9]
	global_load_dwordx2 v[76:77], v[34:35], off offset:512 nt
	global_load_dwordx2 v[78:79], v[34:35], off offset:1024 nt
	global_load_dwordx2 v[80:81], v[34:35], off offset:1536 nt
	global_load_dwordx4 v[68:71], v40, s[8:9]
	global_load_dwordx4 v[72:75], v42, s[8:9]
	v_lshl_add_u64 v[34:35], v[34:35], 0, s[6:7]
	s_waitcnt lgkmcnt(0)
	v_lshlrev_b32_e32 v16, 8, v16
	v_lshlrev_b32_e32 v18, 8, v18
	v_add_u32_e32 v16, v16, v17
	v_add_u32_e32 v18, v18, v19
	v_ashrrev_i32_e32 v17, 31, v16
	v_ashrrev_i32_e32 v19, 31, v18
	v_lshlrev_b64 v[16:17], 12, v[16:17]
	v_lshlrev_b64 v[18:19], 12, v[18:19]
	v_lshl_add_u64 v[16:17], v[30:31], 0, v[16:17]
	v_lshl_add_u64 v[18:19], v[30:31], 0, v[18:19]
	global_load_dwordx2 v[84:85], v[16:17], off nt
	global_load_dwordx2 v[86:87], v[18:19], off nt
	global_load_dwordx2 v[88:89], v[16:17], off offset:512 nt
	global_load_dwordx2 v[90:91], v[18:19], off offset:512 nt
	global_load_dwordx2 v[92:93], v[16:17], off offset:1024 nt
	global_load_dwordx2 v[94:95], v[18:19], off offset:1024 nt
	global_load_dwordx2 v[96:97], v[16:17], off offset:1536 nt
	global_load_dwordx2 v[98:99], v[18:19], off offset:1536 nt
	global_load_dwordx2 v[100:101], v[16:17], off offset:2048 nt
	global_load_dwordx2 v[102:103], v[18:19], off offset:2048 nt
	global_load_dwordx2 v[104:105], v[16:17], off offset:2560 nt
	global_load_dwordx2 v[106:107], v[16:17], off offset:3072 nt
	global_load_dwordx2 v[108:109], v[16:17], off offset:3584 nt
	global_load_dwordx2 v[110:111], v[18:19], off offset:2560 nt
	global_load_dwordx2 v[112:113], v[18:19], off offset:3072 nt
	global_load_dwordx2 v[114:115], v[18:19], off offset:3584 nt
	global_load_dwordx4 v[194:197], v29, s[14:15]
	global_load_dwordx2 v[198:199], v29, s[14:15] offset:16
	s_waitcnt vmcnt(2)
	v_lshlrev_b32_e32 v116, 16, v48
	v_and_b32_e32 v117, 0xffff0000, v48
	v_lshlrev_b32_e32 v48, 16, v49
	v_and_b32_e32 v49, 0xffff0000, v49
	v_lshlrev_b32_e32 v118, 16, v50
	v_and_b32_e32 v119, 0xffff0000, v50
	v_lshlrev_b32_e32 v50, 16, v51
	v_and_b32_e32 v51, 0xffff0000, v51
	v_lshlrev_b32_e32 v120, 16, v52
	v_and_b32_e32 v121, 0xffff0000, v52
	v_lshlrev_b32_e32 v52, 16, v53
	v_and_b32_e32 v53, 0xffff0000, v53
	v_lshlrev_b32_e32 v124, 16, v56
	v_and_b32_e32 v125, 0xffff0000, v56
	v_lshlrev_b32_e32 v132, 16, v86
	v_and_b32_e32 v133, 0xffff0000, v86
	v_lshlrev_b32_e32 v86, 16, v87
	v_and_b32_e32 v87, 0xffff0000, v87
	v_lshlrev_b32_e32 v136, 16, v90
	v_and_b32_e32 v137, 0xffff0000, v90
	v_lshlrev_b32_e32 v90, 16, v91
	v_and_b32_e32 v91, 0xffff0000, v91
	v_lshlrev_b32_e32 v82, 16, v84
	v_and_b32_e32 v83, 0xffff0000, v84
	v_lshlrev_b32_e32 v84, 16, v85
	v_and_b32_e32 v85, 0xffff0000, v85
	v_lshlrev_b32_e32 v134, 16, v88
	v_and_b32_e32 v135, 0xffff0000, v88
	v_lshlrev_b32_e32 v88, 16, v89
	v_and_b32_e32 v89, 0xffff0000, v89
	v_lshlrev_b32_e32 v140, 16, v94
	v_and_b32_e32 v141, 0xffff0000, v94
	v_lshlrev_b32_e32 v94, 16, v95
	v_and_b32_e32 v95, 0xffff0000, v95
	v_lshlrev_b32_e32 v148, 16, v102
	v_and_b32_e32 v149, 0xffff0000, v102
	v_lshlrev_b32_e32 v102, 16, v103
	v_and_b32_e32 v103, 0xffff0000, v103
	v_lshlrev_b32_e32 v156, 16, v112
	v_and_b32_e32 v157, 0xffff0000, v112
	v_lshlrev_b32_e32 v112, 16, v113
	v_and_b32_e32 v113, 0xffff0000, v113
	v_pk_mul_f32 v[86:87], v[46:47], v[86:87] op_sel:[1,0]
	v_pk_mul_f32 v[132:133], v[46:47], v[132:133] op_sel:[1,0]
	v_pk_mul_f32 v[90:91], v[46:47], v[90:91] op_sel:[1,0]
	v_pk_mul_f32 v[136:137], v[46:47], v[136:137] op_sel:[1,0]
	v_lshlrev_b32_e32 v138, 16, v92
	v_and_b32_e32 v139, 0xffff0000, v92
	v_lshlrev_b32_e32 v92, 16, v93
	v_and_b32_e32 v93, 0xffff0000, v93
	v_lshlrev_b32_e32 v144, 16, v98
	v_and_b32_e32 v145, 0xffff0000, v98
	v_lshlrev_b32_e32 v98, 16, v99
	v_and_b32_e32 v99, 0xffff0000, v99
	v_lshlrev_b32_e32 v146, 16, v100
	v_and_b32_e32 v147, 0xffff0000, v100
	v_lshlrev_b32_e32 v100, 16, v101
	v_and_b32_e32 v101, 0xffff0000, v101
	v_lshlrev_b32_e32 v152, 16, v110
	v_and_b32_e32 v153, 0xffff0000, v110
	v_lshlrev_b32_e32 v110, 16, v111
	v_and_b32_e32 v111, 0xffff0000, v111
	v_lshlrev_b32_e32 v154, 16, v106
	v_and_b32_e32 v155, 0xffff0000, v106
	v_lshlrev_b32_e32 v106, 16, v107
	v_and_b32_e32 v107, 0xffff0000, v107
	v_lshlrev_b32_e32 v160, 16, v114
; __device__ __forceinline__ float bf_lo(unsigned w) { return __uint_as_float(w << 16); }
; __device__ __forceinline__ float bf_hi(unsigned w) { return __uint_as_float(w & 0xffff0000u); }
; __device__ __forceinline__ f32x4 ld4_bf(const bf16_t* p) { const u32x2 w = *(const u32x2*)p; return (f32x4){bf_lo(w.x), bf_hi(w.x), bf_lo(w.y), bf_hi(w.y)}; }
; __device__ __forceinline__ float sq4(const f32x4 v) { return (v[0] * v[0] + v[1] * v[1]) + (v[2] * v[2] + v[3] * v[3]); }
; __device__ __forceinline__ void phase_final(const Ctx& P, volatile LAS int* tab, int vcu, int G) {
;     ...
;         f32x4 v[8]; float ss = 0.f;
; #pragma unroll
;         for (int j = 0; j < 8; ++j) { const int c = 4 * lane + 256 * j; const f32x4 x4 = ld4_bf(xr + c), g4 = *(const f32x4*)(g2 + c); const u32x2 a = *(const u32x2*)(y1 + c), b = *(const u32x2*)(y2 + c);
;             const f32x4 ya = (f32x4){bf_lo(a.x), bf_hi(a.x), bf_lo(a.y), bf_hi(a.y)}, yb = (f32x4){bf_lo(b.x), bf_hi(b.x), bf_lo(b.y), bf_hi(b.y)};
;             v[j] = x4 + g4 * (ya * p1 + yb * p2); ss += sq4(v[j]); }
;         ss = wave_sum(ss); const float rstd = __builtin_amdgcn_rsqf(ss * (1.0f / DM) + EPS);
	v_and_b32_e32 v161, 0xffff0000, v114
	v_lshlrev_b32_e32 v114, 16, v115
	v_and_b32_e32 v115, 0xffff0000, v115
	v_pk_mul_f32 v[140:141], v[46:47], v[140:141] op_sel:[1,0]
	v_pk_mul_f32 v[94:95], v[46:47], v[94:95] op_sel:[1,0]
	v_pk_mul_f32 v[102:103], v[46:47], v[102:103] op_sel:[1,0]
	v_pk_mul_f32 v[112:113], v[46:47], v[112:113] op_sel:[1,0]
	v_pk_fma_f32 v[82:83], v[46:47], v[82:83], v[132:133] op_sel_hi:[0,1,1]
	v_pk_fma_f32 v[84:85], v[46:47], v[84:85], v[86:87] op_sel_hi:[0,1,1]
	v_pk_fma_f32 v[86:87], v[46:47], v[134:135], v[136:137] op_sel_hi:[0,1,1]
	v_pk_fma_f32 v[88:89], v[46:47], v[88:89], v[90:91] op_sel_hi:[0,1,1]
	v_lshlrev_b32_e32 v56, 16, v57
	v_and_b32_e32 v57, 0xffff0000, v57
	v_lshlrev_b32_e32 v128, 16, v78
	v_and_b32_e32 v129, 0xffff0000, v78
	v_lshlrev_b32_e32 v78, 16, v79
	v_and_b32_e32 v79, 0xffff0000, v79
	v_lshlrev_b32_e32 v142, 16, v96
	v_and_b32_e32 v143, 0xffff0000, v96
	v_lshlrev_b32_e32 v96, 16, v97
	v_and_b32_e32 v97, 0xffff0000, v97
	v_lshlrev_b32_e32 v150, 16, v104
	v_and_b32_e32 v151, 0xffff0000, v104
	v_lshlrev_b32_e32 v104, 16, v105
	v_and_b32_e32 v105, 0xffff0000, v105
	v_lshlrev_b32_e32 v158, 16, v108
	v_and_b32_e32 v159, 0xffff0000, v108
	v_lshlrev_b32_e32 v108, 16, v109
	v_and_b32_e32 v109, 0xffff0000, v109
	v_pk_mul_f32 v[98:99], v[46:47], v[98:99] op_sel:[1,0]
	v_pk_mul_f32 v[144:145], v[46:47], v[144:145] op_sel:[1,0]
	v_pk_mul_f32 v[148:149], v[46:47], v[148:149] op_sel:[1,0]
	v_pk_mul_f32 v[152:153], v[46:47], v[152:153] op_sel:[1,0]
	v_pk_mul_f32 v[110:111], v[46:47], v[110:111] op_sel:[1,0]
	v_pk_mul_f32 v[156:157], v[46:47], v[156:157] op_sel:[1,0]
	v_pk_mul_f32 v[114:115], v[46:47], v[114:115] op_sel:[1,0]
	v_pk_mul_f32 v[160:161], v[46:47], v[160:161] op_sel:[1,0]
	v_pk_fma_f32 v[90:91], v[46:47], v[92:93], v[94:95] op_sel_hi:[0,1,1]
	v_pk_fma_f32 v[92:93], v[46:47], v[138:139], v[140:141] op_sel_hi:[0,1,1]
	v_pk_fma_f32 v[100:101], v[46:47], v[100:101], v[102:103] op_sel_hi:[0,1,1]
	v_pk_fma_f32 v[106:107], v[46:47], v[106:107], v[112:113] op_sel_hi:[0,1,1]
	v_pk_fma_f32 v[2:3], v[2:3], v[84:85], v[48:49]
	v_pk_fma_f32 v[0:1], v[0:1], v[82:83], v[116:117]
	v_pk_fma_f32 v[10:11], v[10:11], v[88:89], v[50:51]
	v_pk_fma_f32 v[8:9], v[8:9], v[86:87], v[118:119]
	v_lshlrev_b32_e32 v122, 16, v54
	v_and_b32_e32 v123, 0xffff0000, v54
	v_lshlrev_b32_e32 v54, 16, v55
	v_and_b32_e32 v55, 0xffff0000, v55
	v_lshlrev_b32_e32 v130, 16, v80
	v_and_b32_e32 v131, 0xffff0000, v80
	v_lshlrev_b32_e32 v80, 16, v81
	v_and_b32_e32 v81, 0xffff0000, v81
	v_pk_fma_f32 v[94:95], v[46:47], v[142:143], v[144:145] op_sel_hi:[0,1,1]
	v_pk_fma_f32 v[96:97], v[46:47], v[96:97], v[98:99] op_sel_hi:[0,1,1]
	v_pk_fma_f32 v[98:99], v[46:47], v[146:147], v[148:149] op_sel_hi:[0,1,1]
	v_pk_fma_f32 v[102:103], v[46:47], v[104:105], v[110:111] op_sel_hi:[0,1,1]
	v_pk_fma_f32 v[104:105], v[46:47], v[150:151], v[152:153] op_sel_hi:[0,1,1]
	v_pk_fma_f32 v[110:111], v[46:47], v[154:155], v[156:157] op_sel_hi:[0,1,1]
	v_pk_fma_f32 v[112:113], v[46:47], v[158:159], v[160:161] op_sel_hi:[0,1,1]
	v_pk_fma_f32 v[46:47], v[46:47], v[108:109], v[114:115] op_sel_hi:[0,1,1]
	v_pk_fma_f32 v[4:5], v[4:5], v[92:93], v[120:121]
	v_pk_fma_f32 v[6:7], v[6:7], v[90:91], v[52:53]
	v_pk_fma_f32 v[22:23], v[22:23], v[100:101], v[56:57]
	v_pk_fma_f32 v[48:49], v[70:71], v[106:107], v[78:79]
	v_mov_b32_e32 v56, v1
	v_mov_b32_e32 v57, v9
	v_mov_b32_e32 v70, v3
	v_mov_b32_e32 v71, v11
	v_pk_fma_f32 v[14:15], v[14:15], v[96:97], v[54:55]
	v_pk_fma_f32 v[50:51], v[68:69], v[110:111], v[128:129]
	v_pk_fma_f32 v[46:47], v[74:75], v[46:47], v[80:81]
	v_pk_fma_f32 v[52:53], v[72:73], v[112:113], v[130:131]
	v_mov_b32_e32 v54, v0
	v_mov_b32_e32 v55, v8
	v_mov_b32_e32 v68, v2
	v_mov_b32_e32 v69, v10
	v_pk_mul_f32 v[72:73], v[6:7], v[6:7]
	v_pk_mul_f32 v[74:75], v[4:5], v[4:5]
	v_pk_mul_f32 v[56:57], v[56:57], v[56:57]
	v_pk_mul_f32 v[70:71], v[70:71], v[70:71]
	v_lshlrev_b32_e32 v126, 16, v76
	v_and_b32_e32 v127, 0xffff0000, v76
	v_lshlrev_b32_e32 v76, 16, v77
	v_and_b32_e32 v77, 0xffff0000, v77
	v_pk_fma_f32 v[12:13], v[12:13], v[94:95], v[122:123]
	v_pk_mov_b32 v[88:89], v[74:75], v[72:73] op_sel:[1,0]
	v_mov_b32_e32 v75, v73
	v_pk_fma_f32 v[54:55], v[54:55], v[54:55], v[56:57]
	v_pk_fma_f32 v[56:57], v[68:69], v[68:69], v[70:71]
	v_pk_fma_f32 v[20:21], v[20:21], v[98:99], v[124:125]
	v_pk_fma_f32 v[26:27], v[26:27], v[102:103], v[76:77]
	v_mul_f32_e32 v76, v13, v13
	v_mul_f32_e32 v78, v15, v15
	v_pk_add_f32 v[68:69], v[88:89], v[74:75]
	v_pk_add_f32 v[54:55], v[54:55], v[56:57]
	v_pk_fma_f32 v[24:25], v[24:25], v[104:105], v[126:127]
	v_mul_f32_e32 v87, v20, v20
	v_mul_f32_e32 v90, v21, v21
	v_mul_f32_e32 v91, v22, v22
	v_mul_f32_e32 v92, v23, v23
	v_pk_fma_f32 v[72:73], v[12:13], v[12:13], v[76:77] op_sel_hi:[1,1,0]
	v_pk_fma_f32 v[76:77], v[14:15], v[14:15], v[78:79] op_sel_hi:[1,1,0]
	v_pk_add_f32 v[56:57], v[68:69], v[68:69] op_sel:[0,1] op_sel_hi:[1,0]
	v_pk_add_f32 v[54:55], v[54:55], v[54:55] op_sel:[0,1] op_sel_hi:[1,0]
	v_pk_mul_f32 v[80:81], v[26:27], v[26:27]
	v_pk_mul_f32 v[82:83], v[24:25], v[24:25]
	v_mov_b32_e32 v73, v91
	v_mov_b32_e32 v77, v92
	v_mov_b32_e32 v57, v90
	v_mov_b32_e32 v55, v87
	v_pk_mov_b32 v[78:79], v[82:83], v[80:81] op_sel:[1,0]
	v_mov_b32_e32 v83, v81
	v_pk_add_f32 v[68:69], v[72:73], v[76:77]
	v_pk_add_f32 v[54:55], v[54:55], v[56:57]
	v_mul_f32_e32 v84, v51, v51
	v_mul_f32_e32 v86, v49, v49
	v_pk_add_f32 v[70:71], v[78:79], v[82:83]
	v_pk_add_f32 v[54:55], v[54:55], v[68:69]
	v_mul_f32_e32 v93, v52, v52
	v_mul_f32_e32 v94, v53, v53
	v_mul_f32_e32 v95, v46, v46
	v_mul_f32_e32 v96, v47, v47
	v_pk_fma_f32 v[80:81], v[50:51], v[50:51], v[84:85] op_sel_hi:[1,1,0]
	v_pk_fma_f32 v[84:85], v[48:49], v[48:49], v[86:87] op_sel_hi:[1,1,0]
	v_pk_add_f32 v[70:71], v[70:71], v[70:71] op_sel:[0,1] op_sel_hi:[1,0]
	v_pk_add_f32 v[54:55], v[54:55], v[54:55] op_sel:[0,1] op_sel_hi:[1,0]
	v_mov_b32_e32 v81, v95
	v_mov_b32_e32 v85, v96
	v_mov_b32_e32 v71, v94
	v_mov_b32_e32 v55, v93
	v_pk_add_f32 v[72:73], v[80:81], v[84:85]
	v_pk_add_f32 v[54:55], v[54:55], v[70:71]
	s_nop 0
	v_pk_add_f32 v[54:55], v[54:55], v[72:73]
	s_nop 0
	v_add_f32_e32 v54, v54, v55
	ds_bpermute_b32 v55, v58, v54
	s_waitcnt lgkmcnt(0)
; __device__ __forceinline__ void phase_final(const Ctx& P, volatile LAS int* tab, int vcu, int G) {
;     ...
;         ss = wave_sum(ss); const float rstd = __builtin_amdgcn_rsqf(ss * (1.0f / DM) + EPS);
; #pragma unroll
;         for (int j = 0; j < 8; ++j) { const int c = 4 * lane + 256 * j; const f32x4 fg = *(const f32x4*)(P.in[34] + c); *(f32x4*)(P.out + (size_t)row * DM + c) = v[j] * rstd * fg; }
;     }
	v_add_f32_e32 v54, v54, v55
	ds_bpermute_b32 v55, v59, v54
	s_waitcnt lgkmcnt(0)
	v_add_f32_e32 v54, v54, v55
	ds_bpermute_b32 v55, v60, v54
	s_waitcnt lgkmcnt(0)
	v_add_f32_e32 v54, v54, v55
	ds_bpermute_b32 v55, v61, v54
	s_waitcnt lgkmcnt(0)
	v_add_f32_e32 v54, v54, v55
	ds_bpermute_b32 v55, v62, v54
	s_waitcnt lgkmcnt(0)
	v_add_f32_e32 v54, v54, v55
	ds_bpermute_b32 v55, v63, v54
	s_waitcnt lgkmcnt(0)
	v_add_f32_e32 v54, v54, v55
	v_fmamk_f32 v54, v54, 0x3a000000, v67
	v_rsq_f32_e32 v54, v54
	s_nop 0
	v_pk_mul_f32 v[0:1], v[0:1], v[54:55] op_sel_hi:[1,0]
	v_pk_mul_f32 v[2:3], v[2:3], v[54:55] op_sel_hi:[1,0]
	v_pk_mul_f32 v[8:9], v[8:9], v[54:55] op_sel_hi:[1,0]
	v_pk_mul_f32 v[10:11], v[10:11], v[54:55] op_sel_hi:[1,0]
	v_pk_mul_f32 v[4:5], v[4:5], v[54:55] op_sel_hi:[1,0]
	v_pk_mul_f32 v[6:7], v[6:7], v[54:55] op_sel_hi:[1,0]
	v_pk_mul_f32 v[12:13], v[12:13], v[54:55] op_sel_hi:[1,0]
	v_pk_mul_f32 v[14:15], v[14:15], v[54:55] op_sel_hi:[1,0]
	v_pk_mul_f32 v[20:21], v[20:21], v[54:55] op_sel_hi:[1,0]
	v_pk_mul_f32 v[22:23], v[22:23], v[54:55] op_sel_hi:[1,0]
	v_pk_mul_f32 v[24:25], v[24:25], v[54:55] op_sel_hi:[1,0]
	v_pk_mul_f32 v[26:27], v[26:27], v[54:55] op_sel_hi:[1,0]
	v_pk_mul_f32 v[68:69], v[50:51], v[54:55] op_sel_hi:[1,0]
	v_pk_mul_f32 v[70:71], v[48:49], v[54:55] op_sel_hi:[1,0]
	v_pk_mul_f32 v[72:73], v[52:53], v[54:55] op_sel_hi:[1,0]
	v_pk_mul_f32 v[74:75], v[46:47], v[54:55] op_sel_hi:[1,0]
	v_pk_mul_f32 v[0:1], v[162:163], v[0:1]
	v_pk_mul_f32 v[2:3], v[164:165], v[2:3]
	global_store_dwordx4 v[32:33], v[0:3], off offset:-4096 nt
	v_pk_mul_f32 v[8:9], v[166:167], v[8:9]
	v_pk_mul_f32 v[10:11], v[168:169], v[10:11]
	global_store_dwordx4 v[32:33], v[8:11], off offset:-3072 nt
	v_pk_mul_f32 v[4:5], v[170:171], v[4:5]
	v_pk_mul_f32 v[6:7], v[172:173], v[6:7]
	global_store_dwordx4 v[32:33], v[4:7], off offset:-2048 nt
	v_pk_mul_f32 v[12:13], v[174:175], v[12:13]
	v_pk_mul_f32 v[14:15], v[176:177], v[14:15]
	global_store_dwordx4 v[32:33], v[12:15], off offset:-1024 nt
	v_pk_mul_f32 v[20:21], v[178:179], v[20:21]
	v_pk_mul_f32 v[22:23], v[180:181], v[22:23]
	global_store_dwordx4 v[32:33], v[20:23], off nt
	v_pk_mul_f32 v[24:25], v[182:183], v[24:25]
	v_pk_mul_f32 v[26:27], v[184:185], v[26:27]
	global_store_dwordx4 v[32:33], v[24:27], off offset:1024 nt
	v_pk_mul_f32 v[68:69], v[186:187], v[68:69]
	v_pk_mul_f32 v[70:71], v[188:189], v[70:71]
	global_store_dwordx4 v[32:33], v[68:71], off offset:2048 nt
	v_pk_mul_f32 v[72:73], v[190:191], v[72:73]
	v_pk_mul_f32 v[74:75], v[192:193], v[74:75]
	global_store_dwordx4 v[32:33], v[72:75], off offset:3072 nt
	v_lshl_add_u64 v[32:33], v[32:33], 0, s[4:5]
	s_waitcnt vmcnt(8)
	s_cmp_lg_u32 s17, 0
	s_cbranch_scc1 .LBB0_2712
	s_branch .LBB0_2713
